# speedup vs baseline: 1.0620x; 1.0013x over previous
.LBB0_143:
	s_or_b64 exec, exec, s[4:5]
	v_bfe_u32 v11, v3, 6, 4
	v_and_b32_e32 v5, 31, v0
	v_bfe_u32 v7, v0, 5, 1
	v_and_b32_e32 v0, 7, v1
	v_add_u32_e32 v12, v6, v2
	v_cmp_lt_u32_e32 vcc, 7, v11
	v_lshlrev_b32_e32 v13, 5, v0
	s_and_saveexec_b64 s[4:5], vcc
	s_xor_b64 s[4:5], exec, s[4:5]
	s_cbranch_execz .LBB0_145
	v_lshrrev_b32_e32 v0, 6, v3
	v_lshlrev_b32_e32 v0, 4, v0
	v_lshl_or_b32 v1, v12, 8, v13
	v_and_b32_e32 v2, 16, v0
	v_lshlrev_b32_e32 v3, 2, v7
	v_or3_b32 v1, v2, v3, v1
	v_and_b32_e32 v0, 0xe0, v0
	v_lshlrev_b32_e32 v1, 7, v1
	v_or3_b32 v0, v0, v5, v1
	v_add_u32_e32 v2, 0xffffff80, v0
	v_ashrrev_i32_e32 v3, 31, v2
	v_add_u32_e32 v8, 0x80, v0
	v_or_b32_e32 v10, 0x100, v0
	v_add_u32_e32 v12, 0x380, v0
	v_or_b32_e32 v14, 0x400, v0
	v_add_u32_e32 v16, 0x480, v0
	s_waitcnt lgkmcnt(0)
	v_lshl_add_u64 v[2:3], v[2:3], 2, s[2:3]
	v_ashrrev_i32_e32 v1, 31, v0
	v_ashrrev_i32_e32 v9, 31, v8
	v_ashrrev_i32_e32 v11, 31, v10
	v_ashrrev_i32_e32 v13, 31, v12
	v_ashrrev_i32_e32 v15, 31, v14
	v_ashrrev_i32_e32 v17, 31, v16
	v_lshl_add_u64 v[6:7], v[0:1], 2, s[2:3]
	v_lshl_add_u64 v[8:9], v[8:9], 2, s[2:3]
	v_lshl_add_u64 v[10:11], v[10:11], 2, s[2:3]
	v_lshl_add_u64 v[12:13], v[12:13], 2, s[2:3]
	v_lshl_add_u64 v[14:15], v[14:15], 2, s[2:3]
	v_lshl_add_u64 v[16:17], v[16:17], 2, s[2:3]
	global_load_dword v1, v[2:3], off
	global_load_dword v5, v[6:7], off
	global_load_dword v18, v[16:17], off
	global_load_dword v19, v[8:9], off
	global_load_dword v20, v[10:11], off
	global_load_dword v21, v[12:13], off
	global_load_dword v22, v[14:15], off
	v_or_b32_e32 v6, 0x500, v0
	v_ashrrev_i32_e32 v7, 31, v6
	v_lshl_add_u64 v[6:7], v[6:7], 2, s[2:3]
	global_load_dword v3, v[6:7], off
	s_waitcnt vmcnt(6)
	v_cvt_pk_f16_f32 v0, v1, v5
	s_waitcnt vmcnt(5)
	v_cvt_f16_f32_e32 v10, v18
	s_waitcnt vmcnt(3)
	v_cvt_pk_f16_f32 v1, v19, v20
	s_waitcnt vmcnt(1)
	v_cvt_pk_f16_f32 v2, v21, v22
.LBB0_145:
	s_or_saveexec_b64 s[4:5], s[4:5]
	s_waitcnt lgkmcnt(0)
	v_mov_b64_e32 v[8:9], s[2:3]
	s_xor_b64 exec, exec, s[4:5]
	s_cbranch_execz .LBB0_147
	s_load_dwordx2 s[0:1], s[0:1], 0x8
	v_lshlrev_b32_e32 v1, 10, v7
	v_lshl_or_b32 v0, v12, 15, v13
	v_lshl_or_b32 v2, v11, 12, v1
	v_or3_b32 v6, v0, v2, v5
	v_ashrrev_i32_e32 v1, 31, v0
	v_mov_b32_e32 v3, 0
	v_ashrrev_i32_e32 v7, 31, v6
	v_lshl_add_u64 v[0:1], v[0:1], 0, v[2:3]
	v_or_b32_e32 v2, 0x800, v6
	v_or_b32_e32 v10, 0x900, v6
	v_or_b32_e32 v12, 0xa00, v6
	s_waitcnt lgkmcnt(0)
	v_lshl_add_u64 v[8:9], v[6:7], 2, s[0:1]
	v_or_b32_e32 v0, v0, v5
	v_ashrrev_i32_e32 v3, 31, v2
	v_ashrrev_i32_e32 v11, 31, v10
	v_ashrrev_i32_e32 v13, 31, v12
	v_lshl_add_u64 v[0:1], v[0:1], 2, s[0:1]
	v_lshl_add_u64 v[2:3], v[2:3], 2, s[0:1]
	v_lshl_add_u64 v[10:11], v[10:11], 2, s[0:1]
	v_lshl_add_u64 v[12:13], v[12:13], 2, s[0:1]
	global_load_dword v5, v[8:9], off
	global_load_dword v7, v[0:1], off offset:1024
	global_load_dword v14, v[12:13], off
	global_load_dword v15, v[0:1], off offset:2048
	global_load_dword v16, v[0:1], off offset:3072
	global_load_dword v17, v[2:3], off
	global_load_dword v18, v[10:11], off
	v_mov_b64_e32 v[8:9], s[0:1]
	v_or_b32_e32 v6, 0xb00, v6
	v_ashrrev_i32_e32 v21, 31, v6
	v_mov_b32_e32 v20, v6
	v_lshl_add_u64 v[20:21], v[20:21], 2, s[0:1]
	global_load_dword v3, v[20:21], off
	s_waitcnt vmcnt(6)
	v_cvt_pk_f16_f32 v0, v5, v7
	s_waitcnt vmcnt(5)
	v_cvt_f16_f32_e32 v10, v14
	s_waitcnt vmcnt(3)
	v_cvt_pk_f16_f32 v1, v15, v16
	s_waitcnt vmcnt(1)
	v_cvt_pk_f16_f32 v2, v17, v18
.LBB0_147:
	s_or_b64 exec, exec, s[4:5]
	s_mov_b32 s0, 0x5040100
	v_ashrrev_i32_e32 v5, 31, v4
	v_lshl_add_u64 v[4:5], v[4:5], 4, s[6:7]
	s_waitcnt vmcnt(0)
	v_cvt_f16_f32_e32 v3, v3
	v_perm_b32 v3, v3, v10, s0
	global_store_dwordx4 v[4:5], v[0:3], off
